# speedup vs baseline: 1.0080x; 1.0080x over previous
.LBB2_14:
	s_ashr_i32 s51, s50, 31
	s_lshl_b64 s[52:53], s[50:51], 10
	s_add_u32 s52, s10, s52
	s_addc_u32 s53, s11, s53
	v_mov_b32_e32 v162, v1
	s_barrier
	s_add_i32 s78, s70, 0x18000
	v_lshl_add_u64 v[2:3], s[52:53], 0, v[162:163]
	s_ashr_i32 s45, s44, 31
	v_lshl_add_u64 v[2:3], v[2:3], 0, s[20:21]
	s_mov_b32 m0, s78
	v_mov_b32_e32 v162, v1
	s_add_i32 s79, s70, 0x1a000
	s_lshl_b64 s[54:55], s[44:45], 10
	global_load_lds_dwordx4 v[2:3], off
	s_add_u32 s54, s8, s54
	v_lshl_add_u64 v[2:3], s[52:53], 0, v[162:163]
	v_lshl_add_u64 v[2:3], v[2:3], 0, s[22:23]
	s_mov_b32 m0, s79
	s_addc_u32 s55, s9, s55
	v_mov_b32_e32 v162, v1
	s_or_b32 s56, s50, 0x80
	global_load_lds_dwordx4 v[2:3], off
	s_add_i32 s45, s70, 0x8000
	v_lshl_add_u64 v[2:3], s[54:55], 0, v[162:163]
	s_ashr_i32 s57, s56, 31
	v_lshl_add_u64 v[2:3], v[2:3], 0, s[20:21]
	s_mov_b32 m0, s45
	v_mov_b32_e32 v162, v1
	s_add_i32 s80, s70, 0xa000
	s_lshl_b64 s[56:57], s[56:57], 10
	global_load_lds_dwordx4 v[2:3], off
	s_add_u32 s56, s10, s56
	v_lshl_add_u64 v[2:3], s[54:55], 0, v[162:163]
	v_lshl_add_u64 v[2:3], v[2:3], 0, s[22:23]
	s_mov_b32 m0, s80
	s_addc_u32 s57, s11, s57
	v_mov_b32_e32 v162, v1
	global_load_lds_dwordx4 v[2:3], off
	s_add_i32 s82, s70, 0x1c000
	v_lshl_add_u64 v[2:3], s[56:57], 0, v[162:163]
	v_lshl_add_u64 v[2:3], v[2:3], 0, s[20:21]
	s_mov_b32 m0, s82
	v_mov_b32_e32 v162, v1
	global_load_lds_dwordx4 v[2:3], off
	s_add_i32 s84, s70, 0x1e000
	v_lshl_add_u64 v[2:3], s[56:57], 0, v[162:163]
	v_lshl_add_u64 v[2:3], v[2:3], 0, s[22:23]
	s_mov_b32 m0, s84
	v_mov_b32_e32 v50, 0
	global_load_lds_dwordx4 v[2:3], off
	s_waitcnt lgkmcnt(0)
	s_lshr_b32 s86, s44, 10
	s_cmp_eq_u32 s86, 1
	s_cselect_b32 s88, s14, s6
	s_cselect_b32 s89, s15, s7
	s_cmp_eq_u32 s86, 0
	s_cselect_b32 s88, s12, s88
	s_cselect_b32 s89, s13, s89
	s_and_b32 s86, s44, 0x3ff
	s_lshl_b32 s86, s86, 2
	s_add_u32 s88, s88, s86
	s_addc_u32 s89, s89, 0
	v_and_b32_e32 v184, 63, v0
	v_lshlrev_b32_e32 v184, 4, v184
	s_mov_b32 m0, 0x20000
	s_nop 0
	global_load_lds_dwordx4 v184, s[88:89]
	s_waitcnt vmcnt(7)
	s_mov_b32 s85, -2
	s_mov_b64 s[56:57], 0
	v_mov_b32_e32 v51, v50
	v_mov_b32_e32 v52, v50
	v_mov_b32_e32 v53, v50
	v_mov_b32_e32 v66, v50
	v_mov_b32_e32 v67, v50
	v_mov_b32_e32 v68, v50
	v_mov_b32_e32 v69, v50
	v_mov_b32_e32 v82, v50
	v_mov_b32_e32 v83, v50
	v_mov_b32_e32 v84, v50
	v_mov_b32_e32 v85, v50
	v_mov_b32_e32 v86, v50
	v_mov_b32_e32 v87, v50
	v_mov_b32_e32 v88, v50
	v_mov_b32_e32 v89, v50
	v_mov_b32_e32 v98, v50
	v_mov_b32_e32 v99, v50
	v_mov_b32_e32 v100, v50
	v_mov_b32_e32 v101, v50
	v_mov_b32_e32 v110, v50
	v_mov_b32_e32 v111, v50
	v_mov_b32_e32 v112, v50
	v_mov_b32_e32 v113, v50
	v_mov_b32_e32 v122, v50
	v_mov_b32_e32 v123, v50
	v_mov_b32_e32 v124, v50
	v_mov_b32_e32 v125, v50
	v_mov_b32_e32 v126, v50
	v_mov_b32_e32 v127, v50
	v_mov_b32_e32 v128, v50
	v_mov_b32_e32 v129, v50
	v_mov_b32_e32 v118, v50
	v_mov_b32_e32 v119, v50
	v_mov_b32_e32 v120, v50
	v_mov_b32_e32 v121, v50
	v_mov_b32_e32 v114, v50
	v_mov_b32_e32 v115, v50
	v_mov_b32_e32 v116, v50
	v_mov_b32_e32 v117, v50
	v_mov_b32_e32 v106, v50
	v_mov_b32_e32 v107, v50
	v_mov_b32_e32 v108, v50
	v_mov_b32_e32 v109, v50
	v_mov_b32_e32 v102, v50
	v_mov_b32_e32 v103, v50
	v_mov_b32_e32 v104, v50
	v_mov_b32_e32 v105, v50
	v_mov_b32_e32 v94, v50
	v_mov_b32_e32 v95, v50
	v_mov_b32_e32 v96, v50
	v_mov_b32_e32 v97, v50
	v_mov_b32_e32 v90, v50
	v_mov_b32_e32 v91, v50
	v_mov_b32_e32 v92, v50
	v_mov_b32_e32 v93, v50
	v_mov_b32_e32 v78, v50
	v_mov_b32_e32 v79, v50
	v_mov_b32_e32 v80, v50
	v_mov_b32_e32 v81, v50
	v_mov_b32_e32 v74, v50
	v_mov_b32_e32 v75, v50
	v_mov_b32_e32 v76, v50
	v_mov_b32_e32 v77, v50
	v_mov_b32_e32 v62, v50
	v_mov_b32_e32 v63, v50
	v_mov_b32_e32 v64, v50
	v_mov_b32_e32 v65, v50
	v_mov_b32_e32 v54, v50
	v_mov_b32_e32 v55, v50
	v_mov_b32_e32 v56, v50
	v_mov_b32_e32 v57, v50
	v_mov_b32_e32 v42, v50
	v_mov_b32_e32 v43, v50
	v_mov_b32_e32 v44, v50
	v_mov_b32_e32 v45, v50
	v_mov_b32_e32 v34, v50
	v_mov_b32_e32 v35, v50
	v_mov_b32_e32 v36, v50
	v_mov_b32_e32 v37, v50
	v_mov_b32_e32 v26, v50
	v_mov_b32_e32 v27, v50
	v_mov_b32_e32 v28, v50
	v_mov_b32_e32 v29, v50
	v_mov_b32_e32 v18, v50
	v_mov_b32_e32 v19, v50
	v_mov_b32_e32 v20, v50
	v_mov_b32_e32 v21, v50
	v_mov_b32_e32 v10, v50
	v_mov_b32_e32 v11, v50
	v_mov_b32_e32 v12, v50
	v_mov_b32_e32 v13, v50
	v_mov_b32_e32 v2, v50
	v_mov_b32_e32 v3, v50
	v_mov_b32_e32 v4, v50
	v_mov_b32_e32 v5, v50
	v_mov_b32_e32 v70, v50
	v_mov_b32_e32 v71, v50
	v_mov_b32_e32 v72, v50
	v_mov_b32_e32 v73, v50
	v_mov_b32_e32 v58, v50
	v_mov_b32_e32 v59, v50
	v_mov_b32_e32 v60, v50
	v_mov_b32_e32 v61, v50
	v_mov_b32_e32 v46, v50
	v_mov_b32_e32 v47, v50
	v_mov_b32_e32 v48, v50
	v_mov_b32_e32 v49, v50
	v_mov_b32_e32 v38, v50
	v_mov_b32_e32 v39, v50
	v_mov_b32_e32 v40, v50
	v_mov_b32_e32 v41, v50
	v_mov_b32_e32 v30, v50
	v_mov_b32_e32 v31, v50
	v_mov_b32_e32 v32, v50
	v_mov_b32_e32 v33, v50
	v_mov_b32_e32 v22, v50
	v_mov_b32_e32 v23, v50
	v_mov_b32_e32 v24, v50
	v_mov_b32_e32 v25, v50
	v_mov_b32_e32 v14, v50
	v_mov_b32_e32 v15, v50
	v_mov_b32_e32 v16, v50
	v_mov_b32_e32 v17, v50
	v_mov_b32_e32 v6, v50
	v_mov_b32_e32 v7, v50
	v_mov_b32_e32 v8, v50
	v_mov_b32_e32 v9, v50
	s_barrier

.LBB2_21:
	s_or_b64 exec, exec, s[52:53]
	v_mov_b32_e32 v175, v0
	s_addk_i32 s2, 0x100
	v_ashrrev_i32_e32 v130, 2, v175
	v_and_b32_e32 v130, 0xffffffc0, v130
	v_bfe_u32 v172, v175, 4, 2
	s_and_b32 s56, s44, 0xfffffc00
	v_add_u32_e32 v173, s44, v130
	s_cmpk_eq_i32 s56, 0x400
	v_lshlrev_b32_e32 v130, 2, v172
	v_add_u32_e32 v174, 0x80, v173
	s_cselect_b32 s45, s14, s6
	s_cselect_b32 s52, s15, s7
	s_cmpk_lt_u32 s44, 0x400
	v_and_or_b32 v131, v173, s74, v130
	v_and_or_b32 v130, v174, s74, v130
	s_cselect_b32 s53, s13, s52
	s_cselect_b32 s52, s12, s45
	v_lshlrev_b32_e32 v131, 2, v131
	v_lshlrev_b32_e32 v130, 2, v130
	v_lshrrev_b32_e32 v184, 8, v0
	v_bfe_u32 v185, v0, 4, 2
	v_lshlrev_b32_e32 v184, 8, v184
	v_lshl_add_u32 v184, v185, 4, v184
	v_add_u32_e32 v184, 0x20000, v184
	ds_read_b128 v[158:161], v184
	ds_read_b128 v[154:157], v184 offset:64
	ds_read_b128 v[150:153], v184 offset:128
	ds_read_b128 v[146:149], v184 offset:192
	ds_read_b128 v[142:145], v184 offset:512
	ds_read_b128 v[138:141], v184 offset:576
	ds_read_b128 v[134:137], v184 offset:640
	ds_read_b128 v[130:133], v184 offset:704
	s_cmp_ge_i32 s2, s33
	s_waitcnt vmcnt(0) lgkmcnt(0)
	s_cselect_b64 s[52:53], -1, 0
	s_and_b64 vcc, exec, s[52:53]
	s_mov_b32 s54, s50
	s_cbranch_vccnz .LBB2_7
	s_ashr_i32 s44, s2, 31
	s_lshr_b32 s44, s44, 29
	s_add_i32 s54, s2, s44
	s_and_b32 s44, s54, -8
	s_sub_i32 s55, s2, s44
	s_cmp_ge_i32 s55, s63
	s_mov_b64 s[44:45], -1
	s_cbranch_scc0 .LBB2_24
	s_sub_i32 s44, s55, s63
	s_mul_i32 s44, s44, s62
	s_add_i32 s57, s44, s65
	s_mov_b64 s[44:45], 0

.LBB2_26:
	s_endpgm
	s_nop 0
	s_nop 0
	s_nop 0
	s_nop 0
	s_nop 0
	s_nop 0
	s_nop 0
	s_nop 0
	s_nop 0
	s_nop 0
	s_nop 0
	s_nop 0
	s_nop 0
	s_nop 0
	s_nop 0
	s_nop 0
	s_nop 0
	s_nop 0
	s_nop 0
	s_nop 0
	s_nop 0
	s_nop 0
	s_nop 0
	s_nop 0
	s_nop 0
	s_nop 0
	s_nop 0
	s_nop 0
	s_nop 0
	s_nop 0
	s_nop 0
	s_nop 0
	s_nop 0
	s_nop 0
	s_nop 0
	s_nop 0
	s_nop 0
	s_nop 0
	s_nop 0
	s_nop 0
	s_nop 0
	s_nop 0
	s_nop 0
	s_nop 0
	s_nop 0
	s_nop 0
	s_nop 0
	s_nop 0
	s_nop 0
	s_nop 0
	s_nop 0
	s_nop 0
	s_nop 0
	s_nop 0
	s_nop 0
	s_nop 0
	s_nop 0
	s_endpgm

	.amdhsa_kernel _Z6k_gemmILi2EEvPKtS1_PvPKfS4_S4_ii
		.amdhsa_group_segment_fixed_size 1024
		.amdhsa_private_segment_fixed_size 0
		.amdhsa_kernarg_size 56
		.amdhsa_user_sgpr_count 2
		.amdhsa_user_sgpr_dispatch_ptr 0
		.amdhsa_user_sgpr_queue_ptr 0
		.amdhsa_user_sgpr_kernarg_segment_ptr 1
		.amdhsa_user_sgpr_dispatch_id 0
		.amdhsa_user_sgpr_kernarg_preload_length 0
		.amdhsa_user_sgpr_kernarg_preload_offset 0
		.amdhsa_user_sgpr_private_segment_size 0
		.amdhsa_uses_dynamic_stack 0
		.amdhsa_enable_private_segment 0
		.amdhsa_system_sgpr_workgroup_id_x 1
		.amdhsa_system_sgpr_workgroup_id_y 0
		.amdhsa_system_sgpr_workgroup_id_z 0
		.amdhsa_system_sgpr_workgroup_info 0
		.amdhsa_system_vgpr_workitem_id 0
		.amdhsa_next_free_vgpr 256
		.amdhsa_next_free_sgpr 90
		.amdhsa_accum_offset 256
		.amdhsa_reserve_vcc 1
		.amdhsa_float_round_mode_32 0
		.amdhsa_float_round_mode_16_64 0
		.amdhsa_float_denorm_mode_32 3
		.amdhsa_float_denorm_mode_16_64 3
		.amdhsa_dx10_clamp 1
		.amdhsa_ieee_mode 1
		.amdhsa_fp16_overflow 0
		.amdhsa_tg_split 0
		.amdhsa_exception_fp_ieee_invalid_op 0
		.amdhsa_exception_fp_denorm_src 0
		.amdhsa_exception_fp_ieee_div_zero 0
		.amdhsa_exception_fp_ieee_overflow 0
		.amdhsa_exception_fp_ieee_underflow 0
		.amdhsa_exception_fp_ieee_inexact 0
		.amdhsa_exception_int_div_zero 0
	.end_amdhsa_kernel

amdhsa.kernels:
  - .agpr_count:     0
    .args:
      - .actual_access:  read_only
        .address_space:  global
        .offset:         0
        .size:           8
        .value_kind:     global_buffer
      - .actual_access:  write_only
        .address_space:  global
        .offset:         8
        .size:           8
        .value_kind:     global_buffer
      - .offset:         16
        .size:           4
        .value_kind:     by_value
      - .actual_access:  read_only
        .address_space:  global
        .offset:         24
        .size:           8
        .value_kind:     global_buffer
      - .actual_access:  read_only
        .address_space:  global
        .offset:         32
        .size:           8
        .value_kind:     global_buffer
      - .actual_access:  read_only
        .address_space:  global
        .offset:         40
        .size:           8
        .value_kind:     global_buffer
      - .actual_access:  read_only
        .address_space:  global
        .offset:         48
        .size:           8
        .value_kind:     global_buffer
      - .actual_access:  write_only
        .address_space:  global
        .offset:         56
        .size:           8
        .value_kind:     global_buffer
      - .actual_access:  write_only
        .address_space:  global
        .offset:         64
        .size:           8
        .value_kind:     global_buffer
      - .actual_access:  write_only
        .address_space:  global
        .offset:         72
        .size:           8
        .value_kind:     global_buffer
    .group_segment_fixed_size: 16640
    .kernarg_segment_align: 8
    .kernarg_segment_size: 80
    .language:       OpenCL C
    .language_version:
      - 2
      - 0
    .max_flat_workgroup_size: 256
    .name:           _Z6k_prepPK15HIP_vector_typeIfLj4EEPS_IjLj4EEiPKfS6_S6_S6_PtS7_PS_IfLj2EE
    .private_segment_fixed_size: 0
    .sgpr_count:     22
    .sgpr_spill_count: 0
    .symbol:         _Z6k_prepPK15HIP_vector_typeIfLj4EEPS_IjLj4EEiPKfS6_S6_S6_PtS7_PS_IfLj2EE.kd
    .uniform_work_group_size: 1
    .uses_dynamic_stack: false
    .vgpr_count:     45
    .vgpr_spill_count: 0
    .wavefront_size: 64
  - .agpr_count:     0
    .args:
      - .actual_access:  read_only
        .address_space:  global
        .offset:         0
        .size:           8
        .value_kind:     global_buffer
      - .actual_access:  write_only
        .address_space:  global
        .offset:         8
        .size:           8
        .value_kind:     global_buffer
      - .actual_access:  read_only
        .address_space:  global
        .offset:         16
        .size:           8
        .value_kind:     global_buffer
    .group_segment_fixed_size: 36928
    .kernarg_segment_align: 8
    .kernarg_segment_size: 24
    .language:       OpenCL C
    .language_version:
      - 2
      - 0
    .max_flat_workgroup_size: 256
    .name:           _Z5k_fftPKtPtPKDv2_f
    .private_segment_fixed_size: 0
    .sgpr_count:     23
    .sgpr_spill_count: 0
    .symbol:         _Z5k_fftPKtPtPKDv2_f.kd
    .uniform_work_group_size: 1
    .uses_dynamic_stack: false
    .vgpr_count:     128
    .vgpr_spill_count: 0
    .wavefront_size: 64
  - .agpr_count:     0
    .args:
      - .address_space:  global
        .offset:         0
        .size:           8
        .value_kind:     global_buffer
      - .address_space:  global
        .offset:         8
        .size:           8
        .value_kind:     global_buffer
      - .actual_access:  write_only
        .address_space:  global
        .offset:         16
        .size:           8
        .value_kind:     global_buffer
      - .actual_access:  read_only
        .address_space:  global
        .offset:         24
        .size:           8
        .value_kind:     global_buffer
      - .actual_access:  read_only
        .address_space:  global
        .offset:         32
        .size:           8
        .value_kind:     global_buffer
      - .actual_access:  read_only
        .address_space:  global
        .offset:         40
        .size:           8
        .value_kind:     global_buffer
      - .offset:         48
        .size:           4
        .value_kind:     by_value
      - .offset:         52
        .size:           4
        .value_kind:     by_value
    .group_segment_fixed_size: 1024
    .kernarg_segment_align: 8
    .kernarg_segment_size: 56
    .language:       OpenCL C
    .language_version:
      - 2
      - 0
    .max_flat_workgroup_size: 512
    .name:           _Z6k_gemmILi2EEvPKtS1_PvPKfS4_S4_ii
    .private_segment_fixed_size: 0
    .sgpr_count:     96
    .sgpr_spill_count: 0
    .symbol:         _Z6k_gemmILi2EEvPKtS1_PvPKfS4_S4_ii.kd
    .uniform_work_group_size: 1
    .uses_dynamic_stack: false
    .vgpr_count:     256
    .vgpr_spill_count: 0
    .wavefront_size: 64
  - .agpr_count:     0
    .args:
      - .address_space:  global
        .offset:         0
        .size:           8
        .value_kind:     global_buffer
      - .address_space:  global
        .offset:         8
        .size:           8
        .value_kind:     global_buffer
      - .actual_access:  write_only
        .address_space:  global
        .offset:         16
        .size:           8
        .value_kind:     global_buffer
      - .actual_access:  read_only
        .address_space:  global
        .offset:         24
        .size:           8
        .value_kind:     global_buffer
      - .actual_access:  read_only
        .address_space:  global
        .offset:         32
        .size:           8
        .value_kind:     global_buffer
      - .actual_access:  read_only
        .address_space:  global
        .offset:         40
        .size:           8
        .value_kind:     global_buffer
      - .offset:         48
        .size:           4
        .value_kind:     by_value
      - .offset:         52
        .size:           4
        .value_kind:     by_value
    .group_segment_fixed_size: 0
    .kernarg_segment_align: 8
    .kernarg_segment_size: 56
    .language:       OpenCL C
    .language_version:
      - 2
      - 0
    .max_flat_workgroup_size: 512
    .name:           _Z6k_gemmILi4EEvPKtS1_PvPKfS4_S4_ii
    .private_segment_fixed_size: 0
    .sgpr_count:     62
    .sgpr_spill_count: 0
    .symbol:         _Z6k_gemmILi4EEvPKtS1_PvPKfS4_S4_ii.kd
    .uniform_work_group_size: 1
    .uses_dynamic_stack: false
    .vgpr_count:     254
    .vgpr_spill_count: 0
    .wavefront_size: 64
